# E22: E21 with the pipelined act re-quant loop waiting vmcnt(12) in steady state so the previous iteration's 6 stores stay in flight
# baseline (speedup 1.0000x reference)
.LBB0_1291:
	s_or_b64 exec, exec, s[0:1]
	s_waitcnt lgkmcnt(0)
	v_mov_b32_e32 v1, v226
	v_mov_b32_e32 v11, 0
	s_barrier
	global_load_dword v0, v11, s[8:9]
	v_readfirstlane_b32 s0, v1
	s_ashr_i32 s0, s0, 6
	v_readlane_b32 s1, v252, 31
	s_add_i32 s6, s0, s1
	s_waitcnt vmcnt(0)
	v_readfirstlane_b32 s0, v0
	s_lshl_b32 s16, s0, 8
	v_readlane_b32 s0, v252, 2
	v_readlane_b32 s1, v252, 3
	s_add_u32 s10, s0, 0x207f8a00
	s_addc_u32 s11, s1, 0
	s_cmp_ge_i32 s6, s16
	s_cbranch_scc1 .LBB0_1300
	v_and_b32_e32 v0, 63, v1
	v_mbcnt_lo_u32_b32 v1, -1, 0
	v_mbcnt_hi_u32_b32 v2, -1, v1
	v_and_b32_e32 v1, 64, v2
	v_add_u32_e32 v3, 64, v1
	v_xor_b32_e32 v1, 1, v2
	v_cmp_lt_i32_e32 vcc, v1, v3
	v_xor_b32_e32 v4, 2, v2
	v_lshlrev_b32_e32 v10, 2, v0
	v_cndmask_b32_e32 v1, v2, v1, vcc
	v_cmp_lt_i32_e32 vcc, v4, v3
	v_lshl_add_u64 v[12:13], s[12:13], 0, v[10:11]
	v_lshlrev_b32_e32 v10, 5, v0
	v_cndmask_b32_e32 v4, v2, v4, vcc
	v_lshl_add_u64 v[14:15], s[2:3], 0, v[10:11]
	v_lshlrev_b32_e32 v10, 2, v4
	v_xor_b32_e32 v4, 4, v2
	v_cmp_lt_i32_e32 vcc, v4, v3
	v_lshlrev_b32_e32 v1, 2, v1
	v_cmp_eq_u32_e64 s[0:1], 0, v0
	v_cndmask_b32_e32 v4, v2, v4, vcc
	v_lshlrev_b32_e32 v18, 2, v4
	v_xor_b32_e32 v4, 8, v2
	v_cmp_lt_i32_e32 vcc, v4, v3
	s_mov_b32 s17, 0xc0c0400
	v_readlane_b32 s12, v252, 29
	v_cndmask_b32_e32 v4, v2, v4, vcc
	v_lshlrev_b32_e32 v19, 2, v4
	v_xor_b32_e32 v4, 16, v2
	v_cmp_lt_i32_e32 vcc, v4, v3
	v_readlane_b32 s13, v252, 30
	s_nop 0
	v_cndmask_b32_e32 v4, v2, v4, vcc
	v_lshlrev_b32_e32 v20, 2, v4
	v_xor_b32_e32 v4, 32, v2
	v_cmp_lt_i32_e32 vcc, v4, v3
	s_nop 1
	v_cndmask_b32_e32 v2, v2, v4, vcc
	v_lshlrev_b32_e32 v21, 2, v2
	s_mov_b32 s68, 0
	v_readlane_b32 s60, v252, 29
	s_mov_b32 s61, s6
	s_add_i32 s62, s61, s60
	s_cmp_lt_i32 s62, s16
	s_cselect_b32 s62, s62, s61
	s_ashr_i32 s63, s62, 31
	s_mov_b32 s64, s61
	s_ashr_i32 s65, s61, 31
	s_lshl_b64 s[66:67], s[64:65], 8
	v_lshl_add_u64 v[82:83], v[12:13], 0, s[66:67]
	global_load_dword v0, v[82:83], off
	s_lshl_b64 s[66:67], s[64:65], 11
	v_lshl_add_u64 v[36:37], v[14:15], 0, s[66:67]
	s_lshl_b64 s[66:67], s[62:63], 8
	s_waitcnt lgkmcnt(0)
	global_load_dwordx4 v[24:27], v[36:37], off offset:16
	v_lshl_add_u64 v[82:83], v[12:13], 0, s[66:67]
	global_load_dword v22, v[82:83], off
	global_load_dwordx4 v[28:31], v[36:37], off
	s_lshl_b64 s[66:67], s[62:63], 11
	v_lshl_add_u64 v[16:17], v[14:15], 0, s[66:67]
	global_load_dwordx4 v[2:5], v[16:17], off offset:16
	global_load_dwordx4 v[6:9], v[16:17], off
.Lq_top_A:
	s_add_i32 s4, s6, s12
	s_cmp_lt_i32 s4, s16
	s_cselect_b64 s[12:13], -1, 0
	s_ashr_i32 s7, s6, 31
	v_readlane_b32 s60, v252, 29
	s_add_i32 s61, s4, s60
	s_cmp_lt_i32 s61, s16
	s_cselect_b32 s61, s61, s6
	s_add_i32 s62, s61, s60
	s_cmp_lt_i32 s62, s16
	s_cselect_b32 s62, s62, s61
	s_ashr_i32 s63, s62, 31
	s_mov_b32 s64, s61
	s_ashr_i32 s65, s61, 31
	s_lshl_b64 s[66:67], s[64:65], 8
	v_lshl_add_u64 v[82:83], v[12:13], 0, s[66:67]
	global_load_dword v60, v[82:83], off
	s_lshl_b64 s[66:67], s[64:65], 11
	v_lshl_add_u64 v[78:79], v[14:15], 0, s[66:67]
	s_lshl_b64 s[66:67], s[62:63], 8
	s_waitcnt lgkmcnt(0)
	global_load_dwordx4 v[62:65], v[78:79], off offset:16
	v_lshl_add_u64 v[82:83], v[12:13], 0, s[66:67]
	global_load_dword v61, v[82:83], off
	global_load_dwordx4 v[66:69], v[78:79], off
	s_lshl_b64 s[66:67], s[62:63], 11
	v_lshl_add_u64 v[80:81], v[14:15], 0, s[66:67]
	global_load_dwordx4 v[70:73], v[80:81], off offset:16
	global_load_dwordx4 v[74:77], v[80:81], off
	s_cmp_eq_u32 s68, 0
	s_cbranch_scc0 .Lw12_A
	s_waitcnt vmcnt(6)
	s_mov_b32 s68, 1
	s_branch .Lwdone_A
.Lw12_A:
	s_waitcnt vmcnt(12)
.Lwdone_A:
	ds_bpermute_b32 v23, v1, v0
	v_max_f32_e32 v32, v0, v0
	v_cvt_f32_i32_sdwa v33, sext(v24) dst_sel:DWORD dst_unused:UNUSED_PAD src0_sel:BYTE_0
	s_waitcnt lgkmcnt(0)
	v_max_f32_e32 v23, v23, v23
	v_max_f32_e32 v23, v32, v23
	ds_bpermute_b32 v32, v10, v23
	v_cvt_f32_i32_sdwa v34, sext(v24) dst_sel:DWORD dst_unused:UNUSED_PAD src0_sel:BYTE_1
	v_cvt_f32_i32_sdwa v35, sext(v24) dst_sel:DWORD dst_unused:UNUSED_PAD src0_sel:BYTE_2
	v_cvt_f32_i32_sdwa v38, sext(v24) dst_sel:DWORD dst_unused:UNUSED_PAD src0_sel:BYTE_3
	ds_bpermute_b32 v24, v1, v22
	s_waitcnt lgkmcnt(1)
	v_max_f32_e32 v32, v32, v32
	v_max_f32_e32 v23, v23, v32
	ds_bpermute_b32 v32, v18, v23
	v_cvt_f32_i32_sdwa v39, sext(v25) dst_sel:DWORD dst_unused:UNUSED_PAD src0_sel:BYTE_0
	v_cvt_f32_i32_sdwa v40, sext(v25) dst_sel:DWORD dst_unused:UNUSED_PAD src0_sel:BYTE_1
	v_cvt_f32_i32_sdwa v41, sext(v25) dst_sel:DWORD dst_unused:UNUSED_PAD src0_sel:BYTE_2
	v_cvt_f32_i32_sdwa v42, sext(v25) dst_sel:DWORD dst_unused:UNUSED_PAD src0_sel:BYTE_3
	v_max_f32_e32 v25, v22, v22
	s_waitcnt lgkmcnt(1)
	v_max_f32_e32 v24, v24, v24
	v_max_f32_e32 v24, v25, v24
	s_waitcnt lgkmcnt(0)
	v_max_f32_e32 v32, v32, v32
	ds_bpermute_b32 v25, v10, v24
	v_max_f32_e32 v23, v23, v32
	ds_bpermute_b32 v32, v19, v23
	v_cvt_f32_i32_sdwa v43, sext(v26) dst_sel:DWORD dst_unused:UNUSED_PAD src0_sel:BYTE_0
	v_cvt_f32_i32_sdwa v44, sext(v26) dst_sel:DWORD dst_unused:UNUSED_PAD src0_sel:BYTE_1
	s_waitcnt lgkmcnt(1)
	v_max_f32_e32 v25, v25, v25
	v_max_f32_e32 v24, v24, v25
	s_waitcnt lgkmcnt(0)
	v_max_f32_e32 v32, v32, v32
	ds_bpermute_b32 v25, v18, v24
	v_max_f32_e32 v23, v23, v32
	ds_bpermute_b32 v32, v20, v23
	v_cvt_f32_i32_sdwa v45, sext(v26) dst_sel:DWORD dst_unused:UNUSED_PAD src0_sel:BYTE_2
	v_cvt_f32_i32_sdwa v26, sext(v26) dst_sel:DWORD dst_unused:UNUSED_PAD src0_sel:BYTE_3
	s_waitcnt lgkmcnt(1)
	v_max_f32_e32 v25, v25, v25
	v_max_f32_e32 v24, v24, v25
	s_waitcnt lgkmcnt(0)
	v_max_f32_e32 v32, v32, v32
	ds_bpermute_b32 v25, v19, v24
	v_max_f32_e32 v23, v23, v32
	ds_bpermute_b32 v32, v21, v23
	v_cvt_f32_i32_sdwa v46, sext(v28) dst_sel:DWORD dst_unused:UNUSED_PAD src0_sel:BYTE_0
	v_cvt_f32_i32_sdwa v47, sext(v28) dst_sel:DWORD dst_unused:UNUSED_PAD src0_sel:BYTE_1
	s_waitcnt lgkmcnt(1)
	v_max_f32_e32 v25, v25, v25
	v_max_f32_e32 v24, v24, v25
	s_waitcnt lgkmcnt(0)
	v_max_f32_e32 v25, v32, v32
	v_max_f32_e32 v25, v23, v25
	v_rcp_f32_e32 v32, v25
	v_cvt_f32_i32_sdwa v48, sext(v28) dst_sel:DWORD dst_unused:UNUSED_PAD src0_sel:BYTE_2
	v_cvt_f32_i32_sdwa v28, sext(v28) dst_sel:DWORD dst_unused:UNUSED_PAD src0_sel:BYTE_3
	ds_bpermute_b32 v58, v20, v24
	v_mul_f32_e32 v0, v0, v32
	v_cmp_lt_f32_e32 vcc, 0, v25
	v_cvt_f32_i32_sdwa v49, sext(v29) dst_sel:DWORD dst_unused:UNUSED_PAD src0_sel:BYTE_0
	v_cvt_f32_i32_sdwa v50, sext(v29) dst_sel:DWORD dst_unused:UNUSED_PAD src0_sel:BYTE_1
	v_cndmask_b32_e32 v0, 0, v0, vcc
	v_fmaak_f32 v32, v0, v46, 0x4b400000
	v_fmaak_f32 v46, v0, v47, 0x4b400000
	v_fmaak_f32 v47, v0, v48, 0x4b400000
	v_fmaak_f32 v28, v0, v28, 0x4b400000
	v_fmaak_f32 v33, v0, v33, 0x4b400000
	v_fmaak_f32 v34, v0, v34, 0x4b400000
	v_fmaak_f32 v35, v0, v35, 0x4b400000
	v_fmaak_f32 v38, v0, v38, 0x4b400000
	v_fmaak_f32 v39, v0, v39, 0x4b400000
	v_fmaak_f32 v40, v0, v40, 0x4b400000
	v_fmaak_f32 v41, v0, v41, 0x4b400000
	v_fmaak_f32 v42, v0, v42, 0x4b400000
	v_fmaak_f32 v43, v0, v43, 0x4b400000
	v_fmaak_f32 v44, v0, v44, 0x4b400000
	v_fmaak_f32 v45, v0, v45, 0x4b400000
	v_fmaak_f32 v26, v0, v26, 0x4b400000
	v_cvt_f32_i32_sdwa v51, sext(v29) dst_sel:DWORD dst_unused:UNUSED_PAD src0_sel:BYTE_2
	v_cvt_f32_i32_sdwa v29, sext(v29) dst_sel:DWORD dst_unused:UNUSED_PAD src0_sel:BYTE_3
	v_cvt_f32_i32_sdwa v52, sext(v30) dst_sel:DWORD dst_unused:UNUSED_PAD src0_sel:BYTE_0
	v_cvt_f32_i32_sdwa v53, sext(v30) dst_sel:DWORD dst_unused:UNUSED_PAD src0_sel:BYTE_1
	v_cvt_f32_i32_sdwa v54, sext(v30) dst_sel:DWORD dst_unused:UNUSED_PAD src0_sel:BYTE_2
	v_cvt_f32_i32_sdwa v30, sext(v30) dst_sel:DWORD dst_unused:UNUSED_PAD src0_sel:BYTE_3
	v_cvt_f32_i32_sdwa v55, sext(v31) dst_sel:DWORD dst_unused:UNUSED_PAD src0_sel:BYTE_0
	v_cvt_f32_i32_sdwa v56, sext(v31) dst_sel:DWORD dst_unused:UNUSED_PAD src0_sel:BYTE_1
	v_cvt_f32_i32_sdwa v57, sext(v31) dst_sel:DWORD dst_unused:UNUSED_PAD src0_sel:BYTE_2
	v_cvt_f32_i32_sdwa v31, sext(v31) dst_sel:DWORD dst_unused:UNUSED_PAD src0_sel:BYTE_3
	s_waitcnt lgkmcnt(0)
	v_max_f32_e32 v23, v58, v58
	v_perm_b32 v32, v46, v32, s17
	v_perm_b32 v28, v28, v47, s17
	v_perm_b32 v33, v34, v33, s17
	v_perm_b32 v34, v38, v35, s17
	v_perm_b32 v35, v40, v39, s17
	v_perm_b32 v38, v42, v41, s17
	v_perm_b32 v39, v44, v43, s17
	v_perm_b32 v26, v26, v45, s17
	v_max_f32_e32 v23, v24, v23
	v_lshl_or_b32 v28, v28, 16, v32
	v_lshl_or_b32 v32, v34, 16, v33
	v_lshl_or_b32 v33, v38, 16, v35
	v_lshl_or_b32 v34, v26, 16, v39
	v_cvt_f32_i32_sdwa v26, sext(v27) dst_sel:DWORD dst_unused:UNUSED_PAD src0_sel:BYTE_0
	v_cvt_f32_i32_sdwa v35, sext(v27) dst_sel:DWORD dst_unused:UNUSED_PAD src0_sel:BYTE_1
	v_cvt_f32_i32_sdwa v38, sext(v27) dst_sel:DWORD dst_unused:UNUSED_PAD src0_sel:BYTE_2
	v_cvt_f32_i32_sdwa v27, sext(v27) dst_sel:DWORD dst_unused:UNUSED_PAD src0_sel:BYTE_3
	ds_bpermute_b32 v24, v21, v23
	v_fmaak_f32 v48, v0, v49, 0x4b400000
	v_fmaak_f32 v49, v0, v50, 0x4b400000
	v_fmaak_f32 v50, v0, v51, 0x4b400000
	v_fmaak_f32 v29, v0, v29, 0x4b400000
	v_fmaak_f32 v51, v0, v52, 0x4b400000
	v_fmaak_f32 v52, v0, v53, 0x4b400000
	v_fmaak_f32 v53, v0, v54, 0x4b400000
	v_fmaak_f32 v30, v0, v30, 0x4b400000
	v_fmaak_f32 v54, v0, v55, 0x4b400000
	v_fmaak_f32 v55, v0, v56, 0x4b400000
	v_fmaak_f32 v56, v0, v57, 0x4b400000
	v_fmaak_f32 v31, v0, v31, 0x4b400000
	v_perm_b32 v46, v49, v48, s17
	v_perm_b32 v29, v29, v50, s17
	v_perm_b32 v47, v52, v51, s17
	v_perm_b32 v30, v30, v53, s17
	v_perm_b32 v48, v55, v54, s17
	v_perm_b32 v31, v31, v56, s17
	v_fmaak_f32 v26, v0, v26, 0x4b400000
	v_fmaak_f32 v35, v0, v35, 0x4b400000
	v_fmaak_f32 v38, v0, v38, 0x4b400000
	v_fmaak_f32 v0, v0, v27, 0x4b400000
	v_lshl_or_b32 v29, v29, 16, v46
	v_lshl_or_b32 v30, v30, 16, v47
	v_lshl_or_b32 v31, v31, 16, v48
	v_perm_b32 v26, v35, v26, s17
	v_perm_b32 v0, v0, v38, s17
	v_lshl_or_b32 v35, v0, 16, v26
	global_store_dwordx4 v[36:37], v[28:31], off
	global_store_dwordx4 v[36:37], v[32:35], off offset:16
	s_and_saveexec_b64 s[14:15], s[0:1]
	s_cbranch_execz .Lq1297_A
	s_lshl_b64 s[6:7], s[6:7], 2
	v_mul_f32_e32 v0, 0x3c010204, v25
	s_add_u32 s6, s10, s6
	v_cndmask_b32_e32 v0, 1.0, v0, vcc
	s_addc_u32 s7, s11, s7
	global_store_dword v11, v0, s[6:7]

.Lq_top_B:
	s_add_i32 s4, s6, s12
	s_cmp_lt_i32 s4, s16
	s_cselect_b64 s[12:13], -1, 0
	s_ashr_i32 s7, s6, 31
	v_readlane_b32 s60, v252, 29
	s_add_i32 s61, s4, s60
	s_cmp_lt_i32 s61, s16
	s_cselect_b32 s61, s61, s6
	s_add_i32 s62, s61, s60
	s_cmp_lt_i32 s62, s16
	s_cselect_b32 s62, s62, s61
	s_ashr_i32 s63, s62, 31
	s_mov_b32 s64, s61
	s_ashr_i32 s65, s61, 31
	s_lshl_b64 s[66:67], s[64:65], 8
	v_lshl_add_u64 v[82:83], v[12:13], 0, s[66:67]
	global_load_dword v0, v[82:83], off
	s_lshl_b64 s[66:67], s[64:65], 11
	v_lshl_add_u64 v[36:37], v[14:15], 0, s[66:67]
	s_lshl_b64 s[66:67], s[62:63], 8
	s_waitcnt lgkmcnt(0)
	global_load_dwordx4 v[24:27], v[36:37], off offset:16
	v_lshl_add_u64 v[82:83], v[12:13], 0, s[66:67]
	global_load_dword v22, v[82:83], off
	global_load_dwordx4 v[28:31], v[36:37], off
	s_lshl_b64 s[66:67], s[62:63], 11
	v_lshl_add_u64 v[16:17], v[14:15], 0, s[66:67]
	global_load_dwordx4 v[2:5], v[16:17], off offset:16
	global_load_dwordx4 v[6:9], v[16:17], off
	s_waitcnt vmcnt(12)
	ds_bpermute_b32 v23, v1, v60
	v_max_f32_e32 v32, v60, v60
	v_cvt_f32_i32_sdwa v33, sext(v62) dst_sel:DWORD dst_unused:UNUSED_PAD src0_sel:BYTE_0
	s_waitcnt lgkmcnt(0)
	v_max_f32_e32 v23, v23, v23
	v_max_f32_e32 v23, v32, v23
	ds_bpermute_b32 v32, v10, v23
	v_cvt_f32_i32_sdwa v34, sext(v62) dst_sel:DWORD dst_unused:UNUSED_PAD src0_sel:BYTE_1
	v_cvt_f32_i32_sdwa v35, sext(v62) dst_sel:DWORD dst_unused:UNUSED_PAD src0_sel:BYTE_2
	v_cvt_f32_i32_sdwa v38, sext(v62) dst_sel:DWORD dst_unused:UNUSED_PAD src0_sel:BYTE_3
	ds_bpermute_b32 v62, v1, v61
	s_waitcnt lgkmcnt(1)
	v_max_f32_e32 v32, v32, v32
	v_max_f32_e32 v23, v23, v32
	ds_bpermute_b32 v32, v18, v23
	v_cvt_f32_i32_sdwa v39, sext(v63) dst_sel:DWORD dst_unused:UNUSED_PAD src0_sel:BYTE_0
	v_cvt_f32_i32_sdwa v40, sext(v63) dst_sel:DWORD dst_unused:UNUSED_PAD src0_sel:BYTE_1
	v_cvt_f32_i32_sdwa v41, sext(v63) dst_sel:DWORD dst_unused:UNUSED_PAD src0_sel:BYTE_2
	v_cvt_f32_i32_sdwa v42, sext(v63) dst_sel:DWORD dst_unused:UNUSED_PAD src0_sel:BYTE_3
	v_max_f32_e32 v63, v61, v61
	s_waitcnt lgkmcnt(1)
	v_max_f32_e32 v62, v62, v62
	v_max_f32_e32 v62, v63, v62
	s_waitcnt lgkmcnt(0)
	v_max_f32_e32 v32, v32, v32
	ds_bpermute_b32 v63, v10, v62
	v_max_f32_e32 v23, v23, v32
	ds_bpermute_b32 v32, v19, v23
	v_cvt_f32_i32_sdwa v43, sext(v64) dst_sel:DWORD dst_unused:UNUSED_PAD src0_sel:BYTE_0
	v_cvt_f32_i32_sdwa v44, sext(v64) dst_sel:DWORD dst_unused:UNUSED_PAD src0_sel:BYTE_1
	s_waitcnt lgkmcnt(1)
	v_max_f32_e32 v63, v63, v63
	v_max_f32_e32 v62, v62, v63
	s_waitcnt lgkmcnt(0)
	v_max_f32_e32 v32, v32, v32
	ds_bpermute_b32 v63, v18, v62
	v_max_f32_e32 v23, v23, v32
	ds_bpermute_b32 v32, v20, v23
	v_cvt_f32_i32_sdwa v45, sext(v64) dst_sel:DWORD dst_unused:UNUSED_PAD src0_sel:BYTE_2
	v_cvt_f32_i32_sdwa v64, sext(v64) dst_sel:DWORD dst_unused:UNUSED_PAD src0_sel:BYTE_3
	s_waitcnt lgkmcnt(1)
	v_max_f32_e32 v63, v63, v63
	v_max_f32_e32 v62, v62, v63
	s_waitcnt lgkmcnt(0)
	v_max_f32_e32 v32, v32, v32
	ds_bpermute_b32 v63, v19, v62
	v_max_f32_e32 v23, v23, v32
	ds_bpermute_b32 v32, v21, v23
	v_cvt_f32_i32_sdwa v46, sext(v66) dst_sel:DWORD dst_unused:UNUSED_PAD src0_sel:BYTE_0
	v_cvt_f32_i32_sdwa v47, sext(v66) dst_sel:DWORD dst_unused:UNUSED_PAD src0_sel:BYTE_1
	s_waitcnt lgkmcnt(1)
	v_max_f32_e32 v63, v63, v63
	v_max_f32_e32 v62, v62, v63
	s_waitcnt lgkmcnt(0)
	v_max_f32_e32 v63, v32, v32
	v_max_f32_e32 v63, v23, v63
	v_rcp_f32_e32 v32, v63
	v_cvt_f32_i32_sdwa v48, sext(v66) dst_sel:DWORD dst_unused:UNUSED_PAD src0_sel:BYTE_2
	v_cvt_f32_i32_sdwa v66, sext(v66) dst_sel:DWORD dst_unused:UNUSED_PAD src0_sel:BYTE_3
	ds_bpermute_b32 v58, v20, v62
	v_mul_f32_e32 v60, v60, v32
	v_cmp_lt_f32_e32 vcc, 0, v63
	v_cvt_f32_i32_sdwa v49, sext(v67) dst_sel:DWORD dst_unused:UNUSED_PAD src0_sel:BYTE_0
	v_cvt_f32_i32_sdwa v50, sext(v67) dst_sel:DWORD dst_unused:UNUSED_PAD src0_sel:BYTE_1
	v_cndmask_b32_e32 v60, 0, v60, vcc
	v_fmaak_f32 v32, v60, v46, 0x4b400000
	v_fmaak_f32 v46, v60, v47, 0x4b400000
	v_fmaak_f32 v47, v60, v48, 0x4b400000
	v_fmaak_f32 v66, v60, v66, 0x4b400000
	v_fmaak_f32 v33, v60, v33, 0x4b400000
	v_fmaak_f32 v34, v60, v34, 0x4b400000
	v_fmaak_f32 v35, v60, v35, 0x4b400000
	v_fmaak_f32 v38, v60, v38, 0x4b400000
	v_fmaak_f32 v39, v60, v39, 0x4b400000
	v_fmaak_f32 v40, v60, v40, 0x4b400000
	v_fmaak_f32 v41, v60, v41, 0x4b400000
	v_fmaak_f32 v42, v60, v42, 0x4b400000
	v_fmaak_f32 v43, v60, v43, 0x4b400000
	v_fmaak_f32 v44, v60, v44, 0x4b400000
	v_fmaak_f32 v45, v60, v45, 0x4b400000
	v_fmaak_f32 v64, v60, v64, 0x4b400000
	v_cvt_f32_i32_sdwa v51, sext(v67) dst_sel:DWORD dst_unused:UNUSED_PAD src0_sel:BYTE_2
	v_cvt_f32_i32_sdwa v67, sext(v67) dst_sel:DWORD dst_unused:UNUSED_PAD src0_sel:BYTE_3
	v_cvt_f32_i32_sdwa v52, sext(v68) dst_sel:DWORD dst_unused:UNUSED_PAD src0_sel:BYTE_0
	v_cvt_f32_i32_sdwa v53, sext(v68) dst_sel:DWORD dst_unused:UNUSED_PAD src0_sel:BYTE_1
	v_cvt_f32_i32_sdwa v54, sext(v68) dst_sel:DWORD dst_unused:UNUSED_PAD src0_sel:BYTE_2
	v_cvt_f32_i32_sdwa v68, sext(v68) dst_sel:DWORD dst_unused:UNUSED_PAD src0_sel:BYTE_3
	v_cvt_f32_i32_sdwa v55, sext(v69) dst_sel:DWORD dst_unused:UNUSED_PAD src0_sel:BYTE_0
	v_cvt_f32_i32_sdwa v56, sext(v69) dst_sel:DWORD dst_unused:UNUSED_PAD src0_sel:BYTE_1
	v_cvt_f32_i32_sdwa v57, sext(v69) dst_sel:DWORD dst_unused:UNUSED_PAD src0_sel:BYTE_2
	v_cvt_f32_i32_sdwa v69, sext(v69) dst_sel:DWORD dst_unused:UNUSED_PAD src0_sel:BYTE_3
	s_waitcnt lgkmcnt(0)
	v_max_f32_e32 v23, v58, v58
	v_perm_b32 v32, v46, v32, s17
	v_perm_b32 v66, v66, v47, s17
	v_perm_b32 v33, v34, v33, s17
	v_perm_b32 v34, v38, v35, s17
	v_perm_b32 v35, v40, v39, s17
	v_perm_b32 v38, v42, v41, s17
	v_perm_b32 v39, v44, v43, s17
	v_perm_b32 v64, v64, v45, s17
	v_max_f32_e32 v23, v62, v23
	v_lshl_or_b32 v66, v66, 16, v32
	v_lshl_or_b32 v32, v34, 16, v33
	v_lshl_or_b32 v33, v38, 16, v35
	v_lshl_or_b32 v34, v64, 16, v39
	v_cvt_f32_i32_sdwa v64, sext(v65) dst_sel:DWORD dst_unused:UNUSED_PAD src0_sel:BYTE_0
	v_cvt_f32_i32_sdwa v35, sext(v65) dst_sel:DWORD dst_unused:UNUSED_PAD src0_sel:BYTE_1
	v_cvt_f32_i32_sdwa v38, sext(v65) dst_sel:DWORD dst_unused:UNUSED_PAD src0_sel:BYTE_2
	v_cvt_f32_i32_sdwa v65, sext(v65) dst_sel:DWORD dst_unused:UNUSED_PAD src0_sel:BYTE_3
	ds_bpermute_b32 v62, v21, v23
	v_fmaak_f32 v48, v60, v49, 0x4b400000
	v_fmaak_f32 v49, v60, v50, 0x4b400000
	v_fmaak_f32 v50, v60, v51, 0x4b400000
	v_fmaak_f32 v67, v60, v67, 0x4b400000
	v_fmaak_f32 v51, v60, v52, 0x4b400000
	v_fmaak_f32 v52, v60, v53, 0x4b400000
	v_fmaak_f32 v53, v60, v54, 0x4b400000
	v_fmaak_f32 v68, v60, v68, 0x4b400000
	v_fmaak_f32 v54, v60, v55, 0x4b400000
	v_fmaak_f32 v55, v60, v56, 0x4b400000
	v_fmaak_f32 v56, v60, v57, 0x4b400000
	v_fmaak_f32 v69, v60, v69, 0x4b400000
	v_perm_b32 v46, v49, v48, s17
	v_perm_b32 v67, v67, v50, s17
	v_perm_b32 v47, v52, v51, s17
	v_perm_b32 v68, v68, v53, s17
	v_perm_b32 v48, v55, v54, s17
	v_perm_b32 v69, v69, v56, s17
	v_fmaak_f32 v64, v60, v64, 0x4b400000
	v_fmaak_f32 v35, v60, v35, 0x4b400000
	v_fmaak_f32 v38, v60, v38, 0x4b400000
	v_fmaak_f32 v60, v60, v65, 0x4b400000
	v_lshl_or_b32 v67, v67, 16, v46
	v_lshl_or_b32 v68, v68, 16, v47
	v_lshl_or_b32 v69, v69, 16, v48
	v_perm_b32 v64, v35, v64, s17
	v_perm_b32 v60, v60, v38, s17
	v_lshl_or_b32 v35, v60, 16, v64
	global_store_dwordx4 v[78:79], v[66:69], off
	global_store_dwordx4 v[78:79], v[32:35], off offset:16
	s_and_saveexec_b64 s[14:15], s[0:1]
	s_cbranch_execz .Lq1297_B
	s_lshl_b64 s[6:7], s[6:7], 2
	v_mul_f32_e32 v60, 0x3c010204, v63
	s_add_u32 s6, s10, s6
	v_cndmask_b32_e32 v60, 1.0, v60, vcc
	s_addc_u32 s7, s11, s7
	global_store_dword v11, v60, s[6:7]

.LBB0_1300:
	s_waitcnt vmcnt(0)
	s_waitcnt lgkmcnt(0)
	s_barrier
	s_mov_b64 s[0:1], exec
	v_readlane_b32 s4, v252, 11
	v_readlane_b32 s5, v252, 12
	s_and_b64 s[4:5], s[0:1], s[4:5]
	s_mov_b64 exec, s[4:5]
	s_cbranch_execz .LBB0_1352
	s_add_i32 s4, 0, 0x26f20
	v_mov_b32_e32 v0, s4
	s_waitcnt vmcnt(0) expcnt(0) lgkmcnt(0)
	ds_read_b32 v3, v0
	s_add_i32 s4, 0, 0x26f24
	v_mov_b32_e32 v0, s4
	ds_read_b32 v1, v0
	s_waitcnt lgkmcnt(1)
	v_cmp_ne_u32_e32 vcc, 0, v3
	s_cbranch_vccnz .LBB0_1316
	v_readlane_b32 s4, v252, 4
	v_readlane_b32 s5, v252, 5
	s_load_dwordx2 s[12:13], s[4:5], 0x4
	v_readlane_b32 s42, v252, 2
	v_readlane_b32 s43, v252, 3
	s_add_u32 s4, s42, 0x4200
	s_addc_u32 s5, s43, 0
	s_add_u32 s6, s42, 0x4400
	s_addc_u32 s7, s43, 0
	v_readlane_b32 s14, v252, 6
	s_waitcnt lgkmcnt(0)
	s_mul_i32 s51, s12, s14
	s_add_u32 s12, s42, 0x4500
	s_mul_i32 s51, s51, s13
	s_addc_u32 s13, s43, 0
	v_readlane_b32 s15, v252, 7
	s_add_u32 s14, s42, 0x4600
	s_addc_u32 s15, s43, 0
	s_add_u32 s16, s42, 0x4700
	s_addc_u32 s17, s43, 0
	s_add_u32 s18, s42, 0x4800
	s_addc_u32 s19, s43, 0
	s_add_u32 s20, s42, 0x4900
	s_addc_u32 s21, s43, 0
	s_add_u32 s22, s42, 0x4a00
	s_addc_u32 s23, s43, 0
	s_add_u32 s24, s42, 0x4b00
	s_addc_u32 s25, s43, 0
	s_add_u32 s26, s42, 0x4c00
	s_addc_u32 s27, s43, 0
	s_add_u32 s28, s42, 0x4d00
	s_addc_u32 s29, s43, 0
	s_add_u32 s30, s42, 0x4e00
	s_addc_u32 s31, s43, 0
	s_add_u32 s34, s42, 0x4f00
	s_addc_u32 s35, s43, 0
	s_add_u32 s36, s42, 0x5000
	s_addc_u32 s37, s43, 0
	s_add_u32 s38, s42, 0x5100
	s_addc_u32 s39, s43, 0
	s_add_u32 s40, s42, 0x5200
	s_addc_u32 s41, s43, 0
	s_add_u32 s42, s42, 0x5300
	s_addc_u32 s43, s43, 0
	s_mov_b32 s52, 1
	v_mov_b32_e32 v17, 0
	s_branch .LBB0_1304
	s_nop 0
	s_nop 0
	s_nop 0
	s_nop 0
	s_nop 0
	s_nop 0
	s_nop 0
	s_nop 0
	s_nop 0
	s_nop 0
	s_nop 0
	s_nop 0
	s_nop 0
	s_nop 0
